# gemm: per-round w1[3] weight loads issued before the round barrier instead of after it
# baseline (speedup 1.0000x reference)
.LBB2_21:
	global_load_dwordx4 v[22:25], v[90:91], off offset:16
	global_load_dwordx4 v[18:21], v[90:91], off
	s_waitcnt lgkmcnt(0)
	s_barrier
	s_nop 1
	s_cmpk_gt_i32 s23, 0x30d
	s_cbranch_scc1 .LBB2_25
	ds_read2_b64 v[2:5], v108 offset1:1
	v_ashrrev_i32_e32 v97, 31, v96
	v_lshl_add_u64 v[6:7], v[96:97], 4, s[10:11]
	s_waitcnt lgkmcnt(0)
	global_store_dwordx4 v[6:7], v[2:5], off
	s_and_saveexec_b64 s[0:1], s[4:5]
	s_cbranch_execz .LBB2_24
	ds_read2_b32 v[2:3], v109 offset1:1
	ds_read2_b32 v[4:5], v109 offset0:2 offset1:3
	v_ashrrev_i32_e32 v95, 31, v94
	v_lshl_add_u64 v[6:7], v[94:95], 4, s[8:9]
	s_waitcnt lgkmcnt(0)
	global_store_dwordx4 v[6:7], v[2:5], off
